# v3 + expert-weight transposition loads at system scope (sc0 sc1 nt) to keep them out of the L2 the attention K/V re-reads use
# speedup vs baseline: 1.0071x; 1.0014x over previous
.LBB0_861:
	s_and_b32 s36, s80, 1
	s_cmp_eq_u32 s36, 0
	s_cselect_b64 s[92:93], -1, 0
	s_cmp_eq_u32 s36, 1
	s_cselect_b64 s[36:37], -1, 0
	s_ashr_i32 s90, s41, 8
	s_bfe_u32 s66, s41, 0x20006
	s_or_b32 s67, s66, 4
	s_and_b32 s66, s41, 63
	s_ashr_i32 s91, s90, 31
	s_and_b64 vcc, exec, s[36:37]
	s_cbranch_vccnz .LBB0_863
	s_lshl_b64 s[36:37], s[90:91], 23
	s_add_u32 s36, s54, s36
	s_addc_u32 s37, s55, s37
	s_lshl_b32 vcc_lo, s67, 20
	s_and_b32 s37, s37, 0xffff
	v_lshl_or_b32 v2, s66, 7, v161
	s_or_b32 vcc_hi, vcc_lo, 0x2000
	buffer_load_dwordx4 v[4:7], v2, s[36:39], vcc_lo offen sc0 sc1 nt
	buffer_load_dwordx4 v[8:11], v2, s[36:39], vcc_hi offen sc0 sc1 nt
	s_or_b32 vcc_hi, vcc_lo, 0x4000
	buffer_load_dwordx4 v[12:15], v2, s[36:39], vcc_hi offen sc0 sc1 nt
	s_or_b32 vcc_hi, vcc_lo, 0x6000
	buffer_load_dwordx4 v[16:19], v2, s[36:39], vcc_hi offen sc0 sc1 nt
	s_or_b32 vcc_hi, vcc_lo, 0x8000
	buffer_load_dwordx4 v[20:23], v2, s[36:39], vcc_hi offen sc0 sc1 nt
	s_or_b32 vcc_hi, vcc_lo, 0xa000
	buffer_load_dwordx4 v[24:27], v2, s[36:39], vcc_hi offen sc0 sc1 nt
	s_or_b32 vcc_hi, vcc_lo, 0xc000
	buffer_load_dwordx4 v[28:31], v2, s[36:39], vcc_hi offen sc0 sc1 nt
	s_or_b32 vcc_hi, vcc_lo, 0xe000
	buffer_load_dwordx4 v[32:35], v2, s[36:39], vcc_hi offen sc0 sc1 nt
	s_or_b32 vcc_hi, vcc_lo, 0x10000
	buffer_load_dwordx4 v[60:63], v2, s[36:39], vcc_hi offen sc0 sc1 nt
	s_or_b32 vcc_hi, vcc_lo, 0x12000
	buffer_load_dwordx4 v[64:67], v2, s[36:39], vcc_hi offen sc0 sc1 nt
	s_or_b32 vcc_hi, vcc_lo, 0x14000
	buffer_load_dwordx4 v[68:71], v2, s[36:39], vcc_hi offen sc0 sc1 nt
	s_or_b32 vcc_hi, vcc_lo, 0x16000
	buffer_load_dwordx4 v[76:79], v2, s[36:39], vcc_hi offen sc0 sc1 nt
	s_or_b32 vcc_hi, vcc_lo, 0x18000
	buffer_load_dwordx4 v[80:83], v2, s[36:39], vcc_hi offen sc0 sc1 nt
	s_or_b32 vcc_hi, vcc_lo, 0x1a000
	buffer_load_dwordx4 v[96:99], v2, s[36:39], vcc_hi offen sc0 sc1 nt
	s_or_b32 vcc_hi, vcc_lo, 0x1c000
	s_or_b32 vcc_lo, vcc_lo, 0x1e000
	buffer_load_dwordx4 v[100:103], v2, s[36:39], vcc_hi offen sc0 sc1 nt
	buffer_load_dwordx4 v[108:111], v2, s[36:39], vcc_lo offen sc0 sc1 nt

.LBB0_882:
	s_or_b64 exec, exec, s[8:9]
	s_waitcnt lgkmcnt(0)
	s_barrier
	ds_read_b32 v2, v237
	s_waitcnt lgkmcnt(0)
	v_readfirstlane_b32 s2, v2
	s_cmpk_gt_i32 s2, 0x4bf
	s_cselect_b64 s[8:9], -1, 0
	s_and_b64 vcc, exec, s[8:9]
	s_cbranch_vccnz .LBB0_888
	s_mul_hi_i32 s3, s2, 0x6bca1af3
	s_lshr_b32 s10, s3, 31
	s_ashr_i32 s3, s3, 4
	s_add_i32 s12, s3, s10
	s_mul_i32 s3, s12, 38
	s_sub_i32 s2, s2, s3
	s_mov_b64 s[14:15], s[44:45]
	v_mov_b32_e32 v4, v0
	s_add_i32 s3, s2, 2
	s_load_dwordx2 s[10:11], s[14:15], 0xd8
	s_cmp_lt_i32 s2, 32
	s_cselect_b32 s3, s2, s3
	v_readfirstlane_b32 s2, v4
	s_ashr_i32 s2, s2, 6
	v_lshlrev_b32_e32 v2, 1, v4
	v_lshlrev_b32_e32 v4, 2, v4
	s_cmp_gt_i32 s3, 31
	v_and_b32_e32 v2, 0x70, v2
	v_and_b32_e32 v134, 28, v4
	s_mov_b64 s[16:17], -1
	s_cbranch_scc0 .LBB0_885
	s_lshl_b32 s13, s3, 6
	s_add_i32 s13, s13, 0x7ffff800
	s_load_dwordx2 s[16:17], s[14:15], 0xc8
	s_and_b32 s79, s13, 0x7fffff80
	s_lshl_b32 s13, s3, 10
	s_and_b32 s13, s13, 0x400
	s_lshl_b32 s18, s2, 7
	s_add_i32 s18, s18, s13
	s_ashr_i32 s13, s12, 31
	s_lshl_b64 s[24:25], s[12:13], 23
	v_lshlrev_b32_e32 v135, 11, v2
	s_waitcnt lgkmcnt(0)
	s_add_u32 s24, s16, s24
	v_add_u32_e32 v4, s18, v135
	s_addc_u32 s19, s17, s25
	s_lshl_b64 s[16:17], s[12:13], 21
	v_or_b32_e32 v4, v4, v134
	s_lshl_b32 s13, s79, 13
	s_and_b32 s25, s19, 0xffff
	v_lshlrev_b32_e32 v4, 2, v4
	s_or_b32 s19, s13, 0x2000
	buffer_load_dwordx4 v[68:71], v4, s[24:27], s13 offen sc0 sc1 nt
	buffer_load_dwordx4 v[88:91], v4, s[24:27], s19 offen sc0 sc1 nt
	s_or_b32 s40, s13, 0x8000
	s_or_b32 s41, s13, 0xa000
	buffer_load_dwordx4 v[104:107], v4, s[24:27], s40 offen sc0 sc1 nt
	buffer_load_dwordx4 v[116:119], v4, s[24:27], s41 offen sc0 sc1 nt
	s_or_b32 s46, s13, 0x10000
	s_or_b32 s47, s13, 0x12000
	buffer_load_dwordx4 v[72:75], v4, s[24:27], s46 offen sc0 sc1 nt
	buffer_load_dwordx4 v[80:83], v4, s[24:27], s47 offen sc0 sc1 nt
	s_or_b32 s74, s13, 0x18000
	s_or_b32 s75, s13, 0x1a000
	buffer_load_dwordx4 v[76:79], v4, s[24:27], s74 offen sc0 sc1 nt
	buffer_load_dwordx4 v[96:99], v4, s[24:27], s75 offen sc0 sc1 nt
	s_or_b32 s22, s13, 0x4000
	s_or_b32 s33, s13, 0x6000
	s_or_b32 s50, s13, 0x14000
	s_or_b32 s51, s13, 0x16000
	buffer_load_dwordx4 v[100:103], v4, s[24:27], s22 offen sc0 sc1 nt
	buffer_load_dwordx4 v[112:115], v4, s[24:27], s33 offen sc0 sc1 nt
	s_or_b32 s42, s13, 0xc000
	s_or_b32 s43, s13, 0xe000
	buffer_load_dwordx4 v[84:87], v4, s[24:27], s50 offen sc0 sc1 nt
	buffer_load_dwordx4 v[92:95], v4, s[24:27], s51 offen sc0 sc1 nt
	s_or_b32 s76, s13, 0x1c000
	s_or_b32 s77, s13, 0x1e000
	buffer_load_dwordx4 v[124:127], v4, s[24:27], s42 offen sc0 sc1 nt
	buffer_load_dwordx4 v[128:131], v4, s[24:27], s43 offen sc0 sc1 nt
	buffer_load_dwordx4 v[108:111], v4, s[24:27], s76 offen sc0 sc1 nt
	buffer_load_dwordx4 v[120:123], v4, s[24:27], s77 offen sc0 sc1 nt
	s_or_b32 s78, s18, 32
	v_add_u32_e32 v4, s78, v135
	v_or_b32_e32 v4, v4, v134
	v_lshlrev_b32_e32 v16, 2, v4
	buffer_load_dwordx4 v[52:55], v16, s[24:27], s13 offen sc0 sc1 nt
	buffer_load_dwordx4 v[56:59], v16, s[24:27], s19 offen sc0 sc1 nt
	buffer_load_dwordx4 v[60:63], v16, s[24:27], s22 offen sc0 sc1 nt
	buffer_load_dwordx4 v[64:67], v16, s[24:27], s33 offen sc0 sc1 nt
	buffer_load_dwordx4 v[36:39], v16, s[24:27], s40 offen sc0 sc1 nt
	buffer_load_dwordx4 v[40:43], v16, s[24:27], s41 offen sc0 sc1 nt
	buffer_load_dwordx4 v[44:47], v16, s[24:27], s42 offen sc0 sc1 nt
	buffer_load_dwordx4 v[48:51], v16, s[24:27], s43 offen sc0 sc1 nt
	buffer_load_dwordx4 v[20:23], v16, s[24:27], s46 offen sc0 sc1 nt
	buffer_load_dwordx4 v[24:27], v16, s[24:27], s47 offen sc0 sc1 nt
	buffer_load_dwordx4 v[28:31], v16, s[24:27], s50 offen sc0 sc1 nt
	buffer_load_dwordx4 v[32:35], v16, s[24:27], s51 offen sc0 sc1 nt
	buffer_load_dwordx4 v[4:7], v16, s[24:27], s74 offen sc0 sc1 nt
	buffer_load_dwordx4 v[8:11], v16, s[24:27], s75 offen sc0 sc1 nt
	buffer_load_dwordx4 v[12:15], v16, s[24:27], s76 offen sc0 sc1 nt
	s_nop 0
	buffer_load_dwordx4 v[16:19], v16, s[24:27], s77 offen sc0 sc1 nt
	v_mov_b32_e32 v138, v3
	v_mov_b32_e32 v139, v3
	v_mov_b32_e32 v140, v3
	v_mov_b32_e32 v141, v3
	s_add_u32 s16, s10, s16
	s_addc_u32 s17, s11, s17
	s_add_u32 s16, s16, s79
	v_or_b32_e32 v132, s18, v134
	s_addc_u32 s17, s17, 0
	v_lshl_add_u64 v[136:137], s[16:17], 0, v[2:3]
	s_mov_b64 s[16:17], 0x14c00000
	v_ashrrev_i32_e32 v133, 31, v132
	v_lshl_add_u64 v[136:137], v[136:137], 0, s[16:17]
	v_lshlrev_b64 v[142:143], 10, v[132:133]
	v_lshl_add_u64 v[142:143], v[136:137], 0, v[142:143]
	s_or_b32 s16, s18, 64
	s_or_b32 s17, s18, 0x60
	s_waitcnt vmcnt(31)
	v_mul_f32_e32 v68, 0x42800000, v68
	s_waitcnt vmcnt(30)
	v_mul_f32_e32 v88, 0x42800000, v88
	v_cvt_pk_fp8_f32 v138, v68, v88
	s_waitcnt vmcnt(29)
	v_mul_f32_e32 v68, 0x42800000, v104
	s_waitcnt vmcnt(28)
	v_mul_f32_e32 v88, 0x42800000, v116
	v_cvt_pk_fp8_f32 v139, v68, v88
	s_waitcnt vmcnt(27)
	v_mul_f32_e32 v68, 0x42800000, v72
	s_waitcnt vmcnt(26)
	v_mul_f32_e32 v72, 0x42800000, v80
	v_cvt_pk_fp8_f32 v140, v68, v72
	s_waitcnt vmcnt(25)
	v_mul_f32_e32 v68, 0x42800000, v76
	s_waitcnt vmcnt(24)
	v_mul_f32_e32 v72, 0x42800000, v96
	v_cvt_pk_fp8_f32 v141, v68, v72
	v_mul_f32_e32 v68, 0x42800000, v69
	v_mul_f32_e32 v69, 0x42800000, v89
	s_waitcnt vmcnt(23)
	v_mul_f32_e32 v100, 0x42800000, v100
	s_waitcnt vmcnt(22)
	v_mul_f32_e32 v112, 0x42800000, v112
	v_cvt_pk_fp8_f32 v138, v100, v112 op_sel:[0,0,1]
	v_mul_f32_e32 v72, 0x42800000, v101
	s_waitcnt vmcnt(21)
	v_mul_f32_e32 v80, 0x42800000, v84
	s_waitcnt vmcnt(20)
	v_mul_f32_e32 v84, 0x42800000, v92
	v_cvt_pk_fp8_f32 v140, v80, v84 op_sel:[0,0,1]
	s_waitcnt vmcnt(15)
	v_mul_f32_e32 v52, 0x42800000, v52
	v_mul_f32_e32 v100, 0x42800000, v124
	v_mul_f32_e32 v104, 0x42800000, v128
	v_mul_f32_e32 v76, 0x42800000, v108
	v_mul_f32_e32 v80, 0x42800000, v120
	v_cvt_pk_fp8_f32 v139, v100, v104 op_sel:[0,0,1]
	v_cvt_pk_fp8_f32 v141, v76, v80 op_sel:[0,0,1]
	v_mul_f32_e32 v76, 0x42800000, v113
	s_waitcnt vmcnt(14)
	v_mul_f32_e32 v56, 0x42800000, v56
	s_waitcnt vmcnt(11)
	v_mul_f32_e32 v36, 0x42800000, v36
	global_store_dwordx4 v[142:143], v[138:141], off nt
	s_waitcnt vmcnt(11)
	v_mul_f32_e32 v40, 0x42800000, v40
	s_waitcnt vmcnt(8)
	v_mul_f32_e32 v20, 0x42800000, v20
	v_mov_b32_e32 v138, v3
	v_cvt_pk_fp8_f32 v138, v68, v69
	v_mul_f32_e32 v68, 0x42800000, v105
	v_mul_f32_e32 v69, 0x42800000, v117
	v_mov_b32_e32 v139, v3
	v_cvt_pk_fp8_f32 v139, v68, v69
	v_mul_f32_e32 v68, 0x42800000, v73
	v_mul_f32_e32 v69, 0x42800000, v81
	v_mov_b32_e32 v140, v3
	v_cvt_pk_fp8_f32 v140, v68, v69
	v_mul_f32_e32 v68, 0x42800000, v77
	v_mul_f32_e32 v69, 0x42800000, v97
	v_mov_b32_e32 v141, v3
	v_cvt_pk_fp8_f32 v141, v68, v69
	v_cvt_pk_fp8_f32 v138, v72, v76 op_sel:[0,0,1]
	v_mul_f32_e32 v72, 0x42800000, v125
	v_mul_f32_e32 v76, 0x42800000, v129
	v_cvt_pk_fp8_f32 v139, v72, v76 op_sel:[0,0,1]
	v_mul_f32_e32 v72, 0x42800000, v85
	v_mul_f32_e32 v73, 0x42800000, v93
	v_cvt_pk_fp8_f32 v140, v72, v73 op_sel:[0,0,1]
	v_mul_f32_e32 v72, 0x42800000, v109
	v_mul_f32_e32 v73, 0x42800000, v121
	v_cvt_pk_fp8_f32 v141, v72, v73 op_sel:[0,0,1]
	v_or_b32_e32 v68, 1, v132
	v_ashrrev_i32_e32 v69, 31, v68
	v_lshlrev_b64 v[68:69], 10, v[68:69]
	v_lshl_add_u64 v[68:69], v[136:137], 0, v[68:69]
	global_store_dwordx4 v[68:69], v[138:141], off nt
	v_mul_f32_e32 v68, 0x42800000, v70
	v_mul_f32_e32 v69, 0x42800000, v90
	v_mov_b32_e32 v138, v3
	v_cvt_pk_fp8_f32 v138, v68, v69
	v_mul_f32_e32 v68, 0x42800000, v106
	v_mul_f32_e32 v69, 0x42800000, v118
	v_mov_b32_e32 v139, v3
	v_cvt_pk_fp8_f32 v139, v68, v69
	v_mul_f32_e32 v68, 0x42800000, v74
	v_mul_f32_e32 v69, 0x42800000, v82
	v_mov_b32_e32 v140, v3
	v_cvt_pk_fp8_f32 v140, v68, v69
	v_mul_f32_e32 v68, 0x42800000, v78
	v_mul_f32_e32 v69, 0x42800000, v98
	v_mov_b32_e32 v141, v3
	v_mul_f32_e32 v70, 0x42800000, v102
	v_mul_f32_e32 v72, 0x42800000, v114
	v_cvt_pk_fp8_f32 v141, v68, v69
	v_cvt_pk_fp8_f32 v138, v70, v72 op_sel:[0,0,1]
	v_mul_f32_e32 v70, 0x42800000, v126
	v_mul_f32_e32 v72, 0x42800000, v130
	v_cvt_pk_fp8_f32 v139, v70, v72 op_sel:[0,0,1]
	v_mul_f32_e32 v70, 0x42800000, v86
	v_mul_f32_e32 v72, 0x42800000, v94
	v_cvt_pk_fp8_f32 v140, v70, v72 op_sel:[0,0,1]
	v_mul_f32_e32 v70, 0x42800000, v110
	v_mul_f32_e32 v72, 0x42800000, v122
	v_cvt_pk_fp8_f32 v141, v70, v72 op_sel:[0,0,1]
	v_or_b32_e32 v68, 2, v132
	v_ashrrev_i32_e32 v69, 31, v68
	v_lshlrev_b64 v[68:69], 10, v[68:69]
	v_lshl_add_u64 v[68:69], v[136:137], 0, v[68:69]
	global_store_dwordx4 v[68:69], v[138:141], off nt
	v_mul_f32_e32 v69, 0x42800000, v71
	v_mul_f32_e32 v70, 0x42800000, v91
	v_mov_b32_e32 v68, v3
	v_cvt_pk_fp8_f32 v68, v69, v70
	v_mul_f32_e32 v71, 0x42800000, v103
	v_mul_f32_e32 v72, 0x42800000, v115
	v_mul_f32_e32 v70, 0x42800000, v107
	v_cvt_pk_fp8_f32 v68, v71, v72 op_sel:[0,0,1]
	v_mul_f32_e32 v71, 0x42800000, v119
	v_mov_b32_e32 v69, v3
	v_cvt_pk_fp8_f32 v69, v70, v71
	v_mul_f32_e32 v72, 0x42800000, v127
	v_mul_f32_e32 v73, 0x42800000, v131
	v_mul_f32_e32 v71, 0x42800000, v75
	v_cvt_pk_fp8_f32 v69, v72, v73 op_sel:[0,0,1]
	v_mul_f32_e32 v72, 0x42800000, v83
	v_mov_b32_e32 v70, v3
	v_cvt_pk_fp8_f32 v70, v71, v72
	v_mul_f32_e32 v73, 0x42800000, v87
	v_mul_f32_e32 v74, 0x42800000, v95
	v_mul_f32_e32 v72, 0x42800000, v79
	v_cvt_pk_fp8_f32 v70, v73, v74 op_sel:[0,0,1]
	v_mul_f32_e32 v73, 0x42800000, v99
	v_mov_b32_e32 v71, v3
	v_cvt_pk_fp8_f32 v71, v72, v73
	v_mul_f32_e32 v74, 0x42800000, v111
	v_mul_f32_e32 v75, 0x42800000, v123
	v_or_b32_e32 v72, 3, v132
	v_cvt_pk_fp8_f32 v71, v74, v75 op_sel:[0,0,1]
	v_ashrrev_i32_e32 v73, 31, v72
	v_lshlrev_b64 v[72:73], 10, v[72:73]
	v_lshl_add_u64 v[72:73], v[136:137], 0, v[72:73]
	global_store_dwordx4 v[72:73], v[68:71], off nt
	v_mov_b32_e32 v138, v3
	v_mov_b32_e32 v139, v3
	v_add_u32_e32 v68, s16, v135
	s_waitcnt vmcnt(10)
	v_mul_f32_e32 v24, 0x42800000, v24
	v_mov_b32_e32 v140, v3
	s_waitcnt vmcnt(7)
	v_mul_f32_e32 v4, 0x42800000, v4
	s_waitcnt vmcnt(6)
	v_mul_f32_e32 v8, 0x42800000, v8
	v_mov_b32_e32 v141, v3
	v_or_b32_e32 v68, v68, v134
	v_cvt_pk_fp8_f32 v138, v52, v56
	v_cvt_pk_fp8_f32 v139, v36, v40
	v_cvt_pk_fp8_f32 v140, v20, v24
	v_cvt_pk_fp8_f32 v141, v4, v8
	v_lshlrev_b32_e32 v80, 2, v68
	buffer_load_dwordx4 v[116:119], v80, s[24:27], s13 offen sc0 sc1 nt
	buffer_load_dwordx4 v[120:123], v80, s[24:27], s19 offen sc0 sc1 nt
	buffer_load_dwordx4 v[124:127], v80, s[24:27], s22 offen sc0 sc1 nt
	buffer_load_dwordx4 v[128:131], v80, s[24:27], s33 offen sc0 sc1 nt
	buffer_load_dwordx4 v[100:103], v80, s[24:27], s40 offen sc0 sc1 nt
	buffer_load_dwordx4 v[104:107], v80, s[24:27], s41 offen sc0 sc1 nt
	buffer_load_dwordx4 v[108:111], v80, s[24:27], s42 offen sc0 sc1 nt
	buffer_load_dwordx4 v[112:115], v80, s[24:27], s43 offen sc0 sc1 nt
	buffer_load_dwordx4 v[84:87], v80, s[24:27], s46 offen sc0 sc1 nt
	buffer_load_dwordx4 v[88:91], v80, s[24:27], s47 offen sc0 sc1 nt
	buffer_load_dwordx4 v[92:95], v80, s[24:27], s50 offen sc0 sc1 nt
	buffer_load_dwordx4 v[96:99], v80, s[24:27], s51 offen sc0 sc1 nt
	buffer_load_dwordx4 v[68:71], v80, s[24:27], s74 offen sc0 sc1 nt
	buffer_load_dwordx4 v[72:75], v80, s[24:27], s75 offen sc0 sc1 nt
	buffer_load_dwordx4 v[76:79], v80, s[24:27], s76 offen sc0 sc1 nt
	s_nop 0
	buffer_load_dwordx4 v[80:83], v80, s[24:27], s77 offen sc0 sc1 nt
	v_mul_f32_e32 v60, 0x42800000, v60
	v_mul_f32_e32 v64, 0x42800000, v64
	v_mul_f32_e32 v44, 0x42800000, v44
	v_mul_f32_e32 v48, 0x42800000, v48
	v_mul_f32_e32 v28, 0x42800000, v28
	v_mul_f32_e32 v32, 0x42800000, v32
	s_waitcnt vmcnt(21)
	v_mul_f32_e32 v12, 0x42800000, v12
	s_waitcnt vmcnt(20)
	v_mul_f32_e32 v16, 0x42800000, v16
	v_or_b32_e32 v132, s78, v134
	v_cvt_pk_fp8_f32 v138, v60, v64 op_sel:[0,0,1]
	v_cvt_pk_fp8_f32 v139, v44, v48 op_sel:[0,0,1]
	v_cvt_pk_fp8_f32 v140, v28, v32 op_sel:[0,0,1]
	v_cvt_pk_fp8_f32 v141, v12, v16 op_sel:[0,0,1]
	v_ashrrev_i32_e32 v133, 31, v132
	v_lshlrev_b64 v[142:143], 10, v[132:133]
	v_lshl_add_u64 v[142:143], v[136:137], 0, v[142:143]
	global_store_dwordx4 v[142:143], v[138:141], off nt
	v_mul_f32_e32 v4, 0x42800000, v53
	v_mul_f32_e32 v8, 0x42800000, v57
	v_mov_b32_e32 v138, v3
	v_cvt_pk_fp8_f32 v138, v4, v8
	v_mul_f32_e32 v4, 0x42800000, v37
	v_mul_f32_e32 v8, 0x42800000, v41
	v_mov_b32_e32 v139, v3
	v_cvt_pk_fp8_f32 v139, v4, v8
	v_mul_f32_e32 v4, 0x42800000, v21
	v_mul_f32_e32 v8, 0x42800000, v25
	v_mov_b32_e32 v140, v3
	v_cvt_pk_fp8_f32 v140, v4, v8
	v_mul_f32_e32 v4, 0x42800000, v5
	v_mul_f32_e32 v5, 0x42800000, v9
	v_mov_b32_e32 v141, v3
	v_cvt_pk_fp8_f32 v141, v4, v5
	v_mul_f32_e32 v12, 0x42800000, v61
	v_mul_f32_e32 v16, 0x42800000, v65
	v_cvt_pk_fp8_f32 v138, v12, v16 op_sel:[0,0,1]
	v_mul_f32_e32 v12, 0x42800000, v45
	v_mul_f32_e32 v16, 0x42800000, v49
	v_cvt_pk_fp8_f32 v139, v12, v16 op_sel:[0,0,1]
	v_mul_f32_e32 v12, 0x42800000, v29
	v_mul_f32_e32 v16, 0x42800000, v33
	v_mul_f32_e32 v8, 0x42800000, v13
	v_mul_f32_e32 v9, 0x42800000, v17
	v_cvt_pk_fp8_f32 v140, v12, v16 op_sel:[0,0,1]
	v_cvt_pk_fp8_f32 v141, v8, v9 op_sel:[0,0,1]
	v_or_b32_e32 v4, 1, v132
	v_ashrrev_i32_e32 v5, 31, v4
	v_lshlrev_b64 v[4:5], 10, v[4:5]
	v_lshl_add_u64 v[4:5], v[136:137], 0, v[4:5]
	global_store_dwordx4 v[4:5], v[138:141], off nt
	v_mul_f32_e32 v4, 0x42800000, v54
	v_mul_f32_e32 v5, 0x42800000, v58
	v_mov_b32_e32 v138, v3
	v_cvt_pk_fp8_f32 v138, v4, v5
	v_mul_f32_e32 v4, 0x42800000, v38
	v_mul_f32_e32 v5, 0x42800000, v42
	v_mov_b32_e32 v139, v3
	v_cvt_pk_fp8_f32 v139, v4, v5
	v_mul_f32_e32 v4, 0x42800000, v22
	v_mul_f32_e32 v5, 0x42800000, v26
	v_mov_b32_e32 v140, v3
	v_cvt_pk_fp8_f32 v140, v4, v5
	v_mul_f32_e32 v4, 0x42800000, v6
	v_mul_f32_e32 v5, 0x42800000, v10
	v_mov_b32_e32 v141, v3
	v_mul_f32_e32 v8, 0x42800000, v62
	v_mul_f32_e32 v9, 0x42800000, v66
	v_cvt_pk_fp8_f32 v141, v4, v5
	v_cvt_pk_fp8_f32 v138, v8, v9 op_sel:[0,0,1]
	v_mul_f32_e32 v8, 0x42800000, v46
	v_mul_f32_e32 v9, 0x42800000, v50
	v_cvt_pk_fp8_f32 v139, v8, v9 op_sel:[0,0,1]
	v_mul_f32_e32 v8, 0x42800000, v30
	v_mul_f32_e32 v9, 0x42800000, v34
	v_cvt_pk_fp8_f32 v140, v8, v9 op_sel:[0,0,1]
	v_mul_f32_e32 v6, 0x42800000, v14
	v_mul_f32_e32 v8, 0x42800000, v18
	v_cvt_pk_fp8_f32 v141, v6, v8 op_sel:[0,0,1]
	v_or_b32_e32 v4, 2, v132
	v_ashrrev_i32_e32 v5, 31, v4
	v_lshlrev_b64 v[4:5], 10, v[4:5]
	v_lshl_add_u64 v[4:5], v[136:137], 0, v[4:5]
	global_store_dwordx4 v[4:5], v[138:141], off nt
	v_mul_f32_e32 v5, 0x42800000, v55
	v_mul_f32_e32 v6, 0x42800000, v59
	v_mov_b32_e32 v4, v3
	v_cvt_pk_fp8_f32 v4, v5, v6
	v_mul_f32_e32 v8, 0x42800000, v63
	v_mul_f32_e32 v9, 0x42800000, v67
	v_mul_f32_e32 v6, 0x42800000, v39
	v_cvt_pk_fp8_f32 v4, v8, v9 op_sel:[0,0,1]
	v_mul_f32_e32 v8, 0x42800000, v43
	v_mov_b32_e32 v5, v3
	v_cvt_pk_fp8_f32 v5, v6, v8
	v_mul_f32_e32 v9, 0x42800000, v47
	v_mul_f32_e32 v10, 0x42800000, v51
	v_mul_f32_e32 v8, 0x42800000, v23
	v_cvt_pk_fp8_f32 v5, v9, v10 op_sel:[0,0,1]
	v_mul_f32_e32 v9, 0x42800000, v27
	v_mov_b32_e32 v6, v3
	v_cvt_pk_fp8_f32 v6, v8, v9
	v_mul_f32_e32 v8, 0x42800000, v7
	v_mul_f32_e32 v9, 0x42800000, v11
	v_mov_b32_e32 v7, v3
	v_cvt_pk_fp8_f32 v7, v8, v9
	v_mul_f32_e32 v10, 0x42800000, v31
	v_mul_f32_e32 v12, 0x42800000, v35
	v_cvt_pk_fp8_f32 v6, v10, v12 op_sel:[0,0,1]
	v_mul_f32_e32 v10, 0x42800000, v15
	v_mul_f32_e32 v11, 0x42800000, v19
	v_cvt_pk_fp8_f32 v7, v10, v11 op_sel:[0,0,1]
	v_or_b32_e32 v8, 3, v132
	v_ashrrev_i32_e32 v9, 31, v8
	v_lshlrev_b64 v[8:9], 10, v[8:9]
	v_lshl_add_u64 v[8:9], v[136:137], 0, v[8:9]
	global_store_dwordx4 v[8:9], v[4:7], off nt
	s_waitcnt vmcnt(19)
	v_mul_f32_e32 v116, 0x42800000, v116
	s_waitcnt vmcnt(18)
	v_mul_f32_e32 v120, 0x42800000, v120
	v_add_u32_e32 v4, s17, v135
	v_or_b32_e32 v4, v4, v134
	v_lshlrev_b32_e32 v16, 2, v4
	buffer_load_dwordx4 v[52:55], v16, s[24:27], s13 offen sc0 sc1 nt
	buffer_load_dwordx4 v[56:59], v16, s[24:27], s19 offen sc0 sc1 nt
	buffer_load_dwordx4 v[60:63], v16, s[24:27], s22 offen sc0 sc1 nt
	buffer_load_dwordx4 v[64:67], v16, s[24:27], s33 offen sc0 sc1 nt
	buffer_load_dwordx4 v[36:39], v16, s[24:27], s40 offen sc0 sc1 nt
	buffer_load_dwordx4 v[40:43], v16, s[24:27], s41 offen sc0 sc1 nt
	buffer_load_dwordx4 v[44:47], v16, s[24:27], s42 offen sc0 sc1 nt
	buffer_load_dwordx4 v[48:51], v16, s[24:27], s43 offen sc0 sc1 nt
	buffer_load_dwordx4 v[20:23], v16, s[24:27], s46 offen sc0 sc1 nt
	buffer_load_dwordx4 v[24:27], v16, s[24:27], s47 offen sc0 sc1 nt
	buffer_load_dwordx4 v[28:31], v16, s[24:27], s50 offen sc0 sc1 nt
	buffer_load_dwordx4 v[32:35], v16, s[24:27], s51 offen sc0 sc1 nt
	buffer_load_dwordx4 v[4:7], v16, s[24:27], s74 offen sc0 sc1 nt
	buffer_load_dwordx4 v[8:11], v16, s[24:27], s75 offen sc0 sc1 nt
	buffer_load_dwordx4 v[12:15], v16, s[24:27], s76 offen sc0 sc1 nt
	s_nop 0
	buffer_load_dwordx4 v[16:19], v16, s[24:27], s77 offen sc0 sc1 nt
	v_mov_b32_e32 v138, v3
	s_waitcnt vmcnt(31)
	v_mul_f32_e32 v100, 0x42800000, v100
	s_waitcnt vmcnt(30)
	v_mul_f32_e32 v104, 0x42800000, v104
	v_mov_b32_e32 v139, v3
	s_waitcnt vmcnt(27)
	v_mul_f32_e32 v84, 0x42800000, v84
	s_waitcnt vmcnt(26)
	v_mul_f32_e32 v88, 0x42800000, v88
	v_mov_b32_e32 v140, v3
	s_waitcnt vmcnt(23)
	v_mul_f32_e32 v68, 0x42800000, v68
	s_waitcnt vmcnt(22)
	v_mul_f32_e32 v72, 0x42800000, v72
	v_mov_b32_e32 v141, v3
	v_cvt_pk_fp8_f32 v138, v116, v120
	v_cvt_pk_fp8_f32 v139, v100, v104
	v_cvt_pk_fp8_f32 v140, v84, v88
	v_cvt_pk_fp8_f32 v141, v68, v72
	v_mul_f32_e32 v124, 0x42800000, v124
	v_mul_f32_e32 v128, 0x42800000, v128
	v_mul_f32_e32 v108, 0x42800000, v108
	v_mul_f32_e32 v112, 0x42800000, v112
	v_mul_f32_e32 v92, 0x42800000, v92
	v_mul_f32_e32 v96, 0x42800000, v96
	s_waitcnt vmcnt(21)
	v_mul_f32_e32 v76, 0x42800000, v76
	s_waitcnt vmcnt(20)
	v_mul_f32_e32 v80, 0x42800000, v80
	v_or_b32_e32 v132, s16, v134
	v_cvt_pk_fp8_f32 v138, v124, v128 op_sel:[0,0,1]
	v_cvt_pk_fp8_f32 v139, v108, v112 op_sel:[0,0,1]
	v_cvt_pk_fp8_f32 v140, v92, v96 op_sel:[0,0,1]
	v_cvt_pk_fp8_f32 v141, v76, v80 op_sel:[0,0,1]
	v_ashrrev_i32_e32 v133, 31, v132
	v_lshlrev_b64 v[142:143], 10, v[132:133]
	v_lshl_add_u64 v[142:143], v[136:137], 0, v[142:143]
	global_store_dwordx4 v[142:143], v[138:141], off nt
	v_mul_f32_e32 v68, 0x42800000, v117
	v_mul_f32_e32 v72, 0x42800000, v121
	v_mov_b32_e32 v138, v3
	v_cvt_pk_fp8_f32 v138, v68, v72
	v_mul_f32_e32 v68, 0x42800000, v101
	v_mul_f32_e32 v72, 0x42800000, v105
	v_mov_b32_e32 v139, v3
	v_cvt_pk_fp8_f32 v139, v68, v72
	v_mul_f32_e32 v68, 0x42800000, v85
	v_mul_f32_e32 v72, 0x42800000, v89
	v_mov_b32_e32 v140, v3
	v_cvt_pk_fp8_f32 v140, v68, v72
	v_mul_f32_e32 v68, 0x42800000, v69
	v_mul_f32_e32 v69, 0x42800000, v73
	v_mov_b32_e32 v141, v3
	v_cvt_pk_fp8_f32 v141, v68, v69
	v_mul_f32_e32 v76, 0x42800000, v125
	v_mul_f32_e32 v80, 0x42800000, v129
	v_cvt_pk_fp8_f32 v138, v76, v80 op_sel:[0,0,1]
	v_mul_f32_e32 v76, 0x42800000, v109
	v_mul_f32_e32 v80, 0x42800000, v113
	v_cvt_pk_fp8_f32 v139, v76, v80 op_sel:[0,0,1]
	v_mul_f32_e32 v76, 0x42800000, v93
	v_mul_f32_e32 v80, 0x42800000, v97
	v_mul_f32_e32 v72, 0x42800000, v77
	v_mul_f32_e32 v73, 0x42800000, v81
	v_cvt_pk_fp8_f32 v140, v76, v80 op_sel:[0,0,1]
	v_cvt_pk_fp8_f32 v141, v72, v73 op_sel:[0,0,1]
	v_or_b32_e32 v68, 1, v132
	v_ashrrev_i32_e32 v69, 31, v68
	v_lshlrev_b64 v[68:69], 10, v[68:69]
	v_lshl_add_u64 v[68:69], v[136:137], 0, v[68:69]
	global_store_dwordx4 v[68:69], v[138:141], off nt
	v_mul_f32_e32 v68, 0x42800000, v118
	v_mul_f32_e32 v69, 0x42800000, v122
	v_mov_b32_e32 v138, v3
	v_cvt_pk_fp8_f32 v138, v68, v69
	v_mul_f32_e32 v68, 0x42800000, v102
	v_mul_f32_e32 v69, 0x42800000, v106
	v_mov_b32_e32 v139, v3
	v_cvt_pk_fp8_f32 v139, v68, v69
	v_mul_f32_e32 v68, 0x42800000, v86
	v_mul_f32_e32 v69, 0x42800000, v90
	v_mov_b32_e32 v140, v3
	v_cvt_pk_fp8_f32 v140, v68, v69
	v_mul_f32_e32 v68, 0x42800000, v70
	v_mul_f32_e32 v69, 0x42800000, v74
	v_mov_b32_e32 v141, v3
	v_mul_f32_e32 v72, 0x42800000, v126
	v_mul_f32_e32 v73, 0x42800000, v130
	v_cvt_pk_fp8_f32 v141, v68, v69
	v_cvt_pk_fp8_f32 v138, v72, v73 op_sel:[0,0,1]
	v_mul_f32_e32 v72, 0x42800000, v110
	v_mul_f32_e32 v73, 0x42800000, v114
	v_cvt_pk_fp8_f32 v139, v72, v73 op_sel:[0,0,1]
	v_mul_f32_e32 v72, 0x42800000, v94
	v_mul_f32_e32 v73, 0x42800000, v98
	v_cvt_pk_fp8_f32 v140, v72, v73 op_sel:[0,0,1]
	v_mul_f32_e32 v70, 0x42800000, v78
	v_mul_f32_e32 v72, 0x42800000, v82
	v_cvt_pk_fp8_f32 v141, v70, v72 op_sel:[0,0,1]
	v_or_b32_e32 v68, 2, v132
	v_ashrrev_i32_e32 v69, 31, v68
	v_lshlrev_b64 v[68:69], 10, v[68:69]
	v_lshl_add_u64 v[68:69], v[136:137], 0, v[68:69]
	global_store_dwordx4 v[68:69], v[138:141], off nt
	v_mul_f32_e32 v69, 0x42800000, v119
	v_mul_f32_e32 v70, 0x42800000, v123
	v_mov_b32_e32 v68, v3
	v_cvt_pk_fp8_f32 v68, v69, v70
	v_mul_f32_e32 v72, 0x42800000, v127
	v_mul_f32_e32 v73, 0x42800000, v131
	v_mul_f32_e32 v70, 0x42800000, v103
	v_cvt_pk_fp8_f32 v68, v72, v73 op_sel:[0,0,1]
	v_mul_f32_e32 v72, 0x42800000, v107
	v_mov_b32_e32 v69, v3
	v_cvt_pk_fp8_f32 v69, v70, v72
	v_mul_f32_e32 v73, 0x42800000, v111
	v_mul_f32_e32 v74, 0x42800000, v115
	v_mul_f32_e32 v72, 0x42800000, v87
	v_cvt_pk_fp8_f32 v69, v73, v74 op_sel:[0,0,1]
	v_mul_f32_e32 v73, 0x42800000, v91
	v_mov_b32_e32 v70, v3
	v_cvt_pk_fp8_f32 v70, v72, v73
	v_mul_f32_e32 v72, 0x42800000, v71
	v_mul_f32_e32 v73, 0x42800000, v75
	v_mov_b32_e32 v71, v3
	v_cvt_pk_fp8_f32 v71, v72, v73
	v_mul_f32_e32 v74, 0x42800000, v95
	v_mul_f32_e32 v76, 0x42800000, v99
	v_cvt_pk_fp8_f32 v70, v74, v76 op_sel:[0,0,1]
	v_mul_f32_e32 v74, 0x42800000, v79
	v_mul_f32_e32 v75, 0x42800000, v83
	v_cvt_pk_fp8_f32 v71, v74, v75 op_sel:[0,0,1]
	v_or_b32_e32 v72, 3, v132
	v_ashrrev_i32_e32 v73, 31, v72
	v_lshlrev_b64 v[72:73], 10, v[72:73]
	v_lshl_add_u64 v[72:73], v[136:137], 0, v[72:73]
	global_store_dwordx4 v[72:73], v[68:71], off nt
	s_waitcnt vmcnt(19)
	v_mul_f32_e32 v52, 0x42800000, v52
	s_waitcnt vmcnt(18)
	v_mul_f32_e32 v56, 0x42800000, v56
	v_mov_b32_e32 v70, v3
	s_waitcnt vmcnt(15)
	v_mul_f32_e32 v36, 0x42800000, v36
	s_waitcnt vmcnt(14)
	v_mul_f32_e32 v40, 0x42800000, v40
	v_mov_b32_e32 v71, v3
	s_waitcnt vmcnt(11)
	v_mul_f32_e32 v20, 0x42800000, v20
	s_waitcnt vmcnt(10)
	v_mul_f32_e32 v24, 0x42800000, v24
	v_mov_b32_e32 v72, v3
	s_waitcnt vmcnt(7)
	v_mul_f32_e32 v4, 0x42800000, v4
	s_waitcnt vmcnt(6)
	v_mul_f32_e32 v8, 0x42800000, v8
	v_mov_b32_e32 v73, v3
	v_cvt_pk_fp8_f32 v70, v52, v56
	v_cvt_pk_fp8_f32 v71, v36, v40
	v_cvt_pk_fp8_f32 v72, v20, v24
	v_cvt_pk_fp8_f32 v73, v4, v8
	v_mul_f32_e32 v60, 0x42800000, v60
	v_mul_f32_e32 v64, 0x42800000, v64
	v_mul_f32_e32 v44, 0x42800000, v44
	v_mul_f32_e32 v48, 0x42800000, v48
	v_mul_f32_e32 v28, 0x42800000, v28
	v_mul_f32_e32 v32, 0x42800000, v32
	s_waitcnt vmcnt(5)
	v_mul_f32_e32 v12, 0x42800000, v12
	s_waitcnt vmcnt(4)
	v_mul_f32_e32 v16, 0x42800000, v16
	v_or_b32_e32 v68, s17, v134
	v_cvt_pk_fp8_f32 v70, v60, v64 op_sel:[0,0,1]
	v_cvt_pk_fp8_f32 v71, v44, v48 op_sel:[0,0,1]
	v_cvt_pk_fp8_f32 v72, v28, v32 op_sel:[0,0,1]
	v_cvt_pk_fp8_f32 v73, v12, v16 op_sel:[0,0,1]
	v_ashrrev_i32_e32 v69, 31, v68
	v_lshlrev_b64 v[74:75], 10, v[68:69]
	v_lshl_add_u64 v[74:75], v[136:137], 0, v[74:75]
	global_store_dwordx4 v[74:75], v[70:73], off nt
	v_mul_f32_e32 v4, 0x42800000, v53
	v_mul_f32_e32 v8, 0x42800000, v57
	v_mov_b32_e32 v70, v3
	v_cvt_pk_fp8_f32 v70, v4, v8
	v_mul_f32_e32 v4, 0x42800000, v37
	v_mul_f32_e32 v8, 0x42800000, v41
	v_mov_b32_e32 v71, v3
	v_cvt_pk_fp8_f32 v71, v4, v8
	v_mul_f32_e32 v4, 0x42800000, v21
	v_mul_f32_e32 v8, 0x42800000, v25
	v_mov_b32_e32 v72, v3
	v_cvt_pk_fp8_f32 v72, v4, v8
	v_mul_f32_e32 v4, 0x42800000, v5
	v_mul_f32_e32 v5, 0x42800000, v9
	v_mov_b32_e32 v73, v3
	v_cvt_pk_fp8_f32 v73, v4, v5
	v_mul_f32_e32 v12, 0x42800000, v61
	v_mul_f32_e32 v16, 0x42800000, v65
	v_cvt_pk_fp8_f32 v70, v12, v16 op_sel:[0,0,1]
	v_mul_f32_e32 v12, 0x42800000, v45
	v_mul_f32_e32 v16, 0x42800000, v49
	v_cvt_pk_fp8_f32 v71, v12, v16 op_sel:[0,0,1]
	v_mul_f32_e32 v12, 0x42800000, v29
	v_mul_f32_e32 v16, 0x42800000, v33
	v_mul_f32_e32 v8, 0x42800000, v13
	v_mul_f32_e32 v9, 0x42800000, v17
	v_cvt_pk_fp8_f32 v72, v12, v16 op_sel:[0,0,1]
	v_cvt_pk_fp8_f32 v73, v8, v9 op_sel:[0,0,1]
	v_or_b32_e32 v4, 1, v68
	v_ashrrev_i32_e32 v5, 31, v4
	v_lshlrev_b64 v[4:5], 10, v[4:5]
	v_lshl_add_u64 v[4:5], v[136:137], 0, v[4:5]
	global_store_dwordx4 v[4:5], v[70:73], off nt
	v_mul_f32_e32 v4, 0x42800000, v54
	v_mul_f32_e32 v5, 0x42800000, v58
	v_mov_b32_e32 v70, v3
	v_cvt_pk_fp8_f32 v70, v4, v5
	v_mul_f32_e32 v4, 0x42800000, v38
	v_mul_f32_e32 v5, 0x42800000, v42
	v_mov_b32_e32 v71, v3
	v_cvt_pk_fp8_f32 v71, v4, v5
	v_mul_f32_e32 v4, 0x42800000, v22
	v_mul_f32_e32 v5, 0x42800000, v26
	v_mov_b32_e32 v72, v3
	v_cvt_pk_fp8_f32 v72, v4, v5
	v_mul_f32_e32 v4, 0x42800000, v6
	v_mul_f32_e32 v5, 0x42800000, v10
	v_mov_b32_e32 v73, v3
	v_mul_f32_e32 v8, 0x42800000, v62
	v_mul_f32_e32 v9, 0x42800000, v66
	v_cvt_pk_fp8_f32 v73, v4, v5
	v_cvt_pk_fp8_f32 v70, v8, v9 op_sel:[0,0,1]
	v_mul_f32_e32 v8, 0x42800000, v46
	v_mul_f32_e32 v9, 0x42800000, v50
	v_cvt_pk_fp8_f32 v71, v8, v9 op_sel:[0,0,1]
	v_mul_f32_e32 v8, 0x42800000, v30
	v_mul_f32_e32 v9, 0x42800000, v34
	v_cvt_pk_fp8_f32 v72, v8, v9 op_sel:[0,0,1]
	v_mul_f32_e32 v6, 0x42800000, v14
	v_mul_f32_e32 v8, 0x42800000, v18
	v_cvt_pk_fp8_f32 v73, v6, v8 op_sel:[0,0,1]
	v_or_b32_e32 v4, 2, v68
	v_ashrrev_i32_e32 v5, 31, v4
	v_lshlrev_b64 v[4:5], 10, v[4:5]
	v_lshl_add_u64 v[4:5], v[136:137], 0, v[4:5]
	global_store_dwordx4 v[4:5], v[70:73], off nt
	v_mul_f32_e32 v5, 0x42800000, v55
	v_mul_f32_e32 v6, 0x42800000, v59
	v_mov_b32_e32 v4, v3
	v_cvt_pk_fp8_f32 v4, v5, v6
	v_mul_f32_e32 v8, 0x42800000, v63
	v_mul_f32_e32 v9, 0x42800000, v67
	v_mul_f32_e32 v6, 0x42800000, v39
	v_cvt_pk_fp8_f32 v4, v8, v9 op_sel:[0,0,1]
	v_mul_f32_e32 v8, 0x42800000, v43
	v_mov_b32_e32 v5, v3
	v_cvt_pk_fp8_f32 v5, v6, v8
	v_mul_f32_e32 v9, 0x42800000, v47
	v_mul_f32_e32 v10, 0x42800000, v51
	v_mul_f32_e32 v8, 0x42800000, v23
	v_cvt_pk_fp8_f32 v5, v9, v10 op_sel:[0,0,1]
	v_mul_f32_e32 v9, 0x42800000, v27
	v_mov_b32_e32 v6, v3
	v_cvt_pk_fp8_f32 v6, v8, v9
	v_mul_f32_e32 v8, 0x42800000, v7
	v_mul_f32_e32 v9, 0x42800000, v11
	v_mov_b32_e32 v7, v3
	v_cvt_pk_fp8_f32 v7, v8, v9
	v_mul_f32_e32 v10, 0x42800000, v31
	v_mul_f32_e32 v12, 0x42800000, v35
	v_cvt_pk_fp8_f32 v6, v10, v12 op_sel:[0,0,1]
	v_mul_f32_e32 v10, 0x42800000, v15
	v_mul_f32_e32 v11, 0x42800000, v19
	v_cvt_pk_fp8_f32 v7, v10, v11 op_sel:[0,0,1]
	v_or_b32_e32 v8, 3, v68
	s_mov_b64 s[16:17], 0
.LBB0_885:
	s_andn2_b64 vcc, exec, s[16:17]
	s_mov_b64 s[16:17], 10
	s_cbranch_vccnz .LBB0_887
	s_lshl_b32 s13, s3, 7
	s_and_b32 s50, s13, 0x780
	s_cmp_lt_u32 s3, 16
	s_movk_i32 s13, 0xb8
	s_cselect_b32 s13, s13, 0xc0
	s_add_u32 s14, s14, s13
	s_addc_u32 s15, s15, 0
	s_load_dwordx2 s[14:15], s[14:15], 0x0
	s_ashr_i32 s13, s12, 31
	s_lshl_b64 s[16:17], s[12:13], 23
	v_lshlrev_b32_e32 v4, 10, v2
	v_mov_b32_e32 v135, v3
	s_waitcnt lgkmcnt(0)
	s_add_u32 s24, s14, s16
	s_addc_u32 s14, s15, s17
	s_lshl_b32 s51, s2, 7
	s_lshl_b32 s3, s3, 3
	v_add_u32_e32 v5, s51, v4
	s_and_b32 s74, s3, 0xffffff80
	v_or_b32_e32 v5, v5, v134
	s_lshl_b32 s3, s50, 12
	s_and_b32 s25, s14, 0xffff
	v_lshlrev_b32_e32 v5, 2, v5
	s_or_b32 s14, s3, 0x1000
	buffer_load_dwordx4 v[68:71], v5, s[24:27], s3 offen sc0 sc1 nt
	buffer_load_dwordx4 v[76:79], v5, s[24:27], s14 offen sc0 sc1 nt
	s_or_b32 s16, s3, 0x3000
	s_or_b32 s17, s3, 0x4000
	s_or_b32 s18, s3, 0x5000
	buffer_load_dwordx4 v[104:107], v5, s[24:27], s16 offen sc0 sc1 nt
	buffer_load_dwordx4 v[84:87], v5, s[24:27], s17 offen sc0 sc1 nt
	buffer_load_dwordx4 v[108:111], v5, s[24:27], s18 offen sc0 sc1 nt
	s_or_b32 s22, s3, 0x7000
	s_lshl_b32 s75, s2, 8
	s_or_b32 s2, s3, 0x8000
	s_or_b32 s33, s3, 0x9000
	buffer_load_dwordx4 v[128:131], v5, s[24:27], s22 offen sc0 sc1 nt
	buffer_load_dwordx4 v[92:95], v5, s[24:27], s33 offen sc0 sc1 nt
	buffer_load_dwordx4 v[72:75], v5, s[24:27], s2 offen sc0 sc1 nt
	s_or_b32 s42, s3, 0xc000
	s_or_b32 s43, s3, 0xd000
	s_or_b32 s15, s3, 0x2000
	buffer_load_dwordx4 v[88:91], v5, s[24:27], s42 offen sc0 sc1 nt
	buffer_load_dwordx4 v[100:103], v5, s[24:27], s43 offen sc0 sc1 nt
	buffer_load_dwordx4 v[80:83], v5, s[24:27], s15 offen sc0 sc1 nt
	s_or_b32 s19, s3, 0x6000
	buffer_load_dwordx4 v[116:119], v5, s[24:27], s19 offen sc0 sc1 nt
	s_or_b32 s40, s3, 0xa000
	s_or_b32 s41, s3, 0xb000
	buffer_load_dwordx4 v[96:99], v5, s[24:27], s40 offen sc0 sc1 nt
	buffer_load_dwordx4 v[120:123], v5, s[24:27], s41 offen sc0 sc1 nt
	s_or_b32 s46, s3, 0xe000
	s_or_b32 s47, s3, 0xf000
	buffer_load_dwordx4 v[112:115], v5, s[24:27], s46 offen sc0 sc1 nt
	buffer_load_dwordx4 v[124:127], v5, s[24:27], s47 offen sc0 sc1 nt
	v_or_b32_e32 v5, s51, v134
	v_add_lshl_u32 v140, v5, v4, 2
	buffer_load_dwordx4 v[52:55], v140, s[24:27], s3 offen offset:128 sc0 sc1 nt
	buffer_load_dwordx4 v[56:59], v140, s[24:27], s14 offen offset:128 sc0 sc1 nt
	buffer_load_dwordx4 v[60:63], v140, s[24:27], s15 offen offset:128 sc0 sc1 nt
	buffer_load_dwordx4 v[64:67], v140, s[24:27], s16 offen offset:128 sc0 sc1 nt
	buffer_load_dwordx4 v[36:39], v140, s[24:27], s17 offen offset:128 sc0 sc1 nt
	buffer_load_dwordx4 v[40:43], v140, s[24:27], s18 offen offset:128 sc0 sc1 nt
	buffer_load_dwordx4 v[44:47], v140, s[24:27], s19 offen offset:128 sc0 sc1 nt
	buffer_load_dwordx4 v[48:51], v140, s[24:27], s22 offen offset:128 sc0 sc1 nt
	buffer_load_dwordx4 v[20:23], v140, s[24:27], s2 offen offset:128 sc0 sc1 nt
	buffer_load_dwordx4 v[24:27], v140, s[24:27], s33 offen offset:128 sc0 sc1 nt
	buffer_load_dwordx4 v[28:31], v140, s[24:27], s40 offen offset:128 sc0 sc1 nt
	buffer_load_dwordx4 v[32:35], v140, s[24:27], s41 offen offset:128 sc0 sc1 nt
	buffer_load_dwordx4 v[4:7], v140, s[24:27], s42 offen offset:128 sc0 sc1 nt
	buffer_load_dwordx4 v[8:11], v140, s[24:27], s43 offen offset:128 sc0 sc1 nt
	buffer_load_dwordx4 v[12:15], v140, s[24:27], s46 offen offset:128 sc0 sc1 nt
	buffer_load_dwordx4 v[16:19], v140, s[24:27], s47 offen offset:128 sc0 sc1 nt
	s_lshl_b64 s[12:13], s[12:13], 22
	s_add_u32 s10, s10, s12
	s_addc_u32 s11, s11, s13
	s_add_i32 s75, s75, s74
	s_add_u32 s10, s10, s50
	s_addc_u32 s11, s11, 0
	v_lshl_add_u64 v[132:133], s[10:11], 0, v[2:3]
	s_mov_b64 s[10:11], 0x4c00000
	v_lshl_add_u64 v[136:137], v[132:133], 0, s[10:11]
	v_mov_b32_e32 v132, v3
	v_mov_b32_e32 v133, v3
	v_or_b32_e32 v138, s75, v134
	v_mov_b32_e32 v134, v3
	v_ashrrev_i32_e32 v139, 31, v138
	v_lshlrev_b64 v[142:143], 11, v[138:139]
	v_lshl_add_u64 v[142:143], v[136:137], 0, v[142:143]
	s_waitcnt vmcnt(31)
	v_mul_f32_e32 v2, 0x42800000, v68
	s_waitcnt vmcnt(30)
	v_mul_f32_e32 v68, 0x42800000, v76
	v_cvt_pk_fp8_f32 v132, v2, v68
	s_waitcnt vmcnt(28)
	v_mul_f32_e32 v2, 0x42800000, v84
	s_waitcnt vmcnt(27)
	v_mul_f32_e32 v68, 0x42800000, v108
	v_cvt_pk_fp8_f32 v133, v2, v68
	s_waitcnt vmcnt(25)
	v_mul_f32_e32 v68, 0x42800000, v92
	s_waitcnt vmcnt(24)
	v_mul_f32_e32 v2, 0x42800000, v72
	v_cvt_pk_fp8_f32 v134, v2, v68
	s_waitcnt vmcnt(23)
	v_mul_f32_e32 v2, 0x42800000, v88
	s_waitcnt vmcnt(22)
	v_mul_f32_e32 v68, 0x42800000, v100
	s_waitcnt vmcnt(21)
	v_mul_f32_e32 v76, 0x42800000, v80
	v_mul_f32_e32 v80, 0x42800000, v104
	v_cvt_pk_fp8_f32 v135, v2, v68
	v_cvt_pk_fp8_f32 v132, v76, v80 op_sel:[0,0,1]
	s_waitcnt vmcnt(20)
	v_mul_f32_e32 v76, 0x42800000, v116
	v_mul_f32_e32 v80, 0x42800000, v128
	v_cvt_pk_fp8_f32 v133, v76, v80 op_sel:[0,0,1]
	s_waitcnt vmcnt(19)
	v_mul_f32_e32 v72, 0x42800000, v96
	s_waitcnt vmcnt(18)
	v_mul_f32_e32 v76, 0x42800000, v120
	v_cvt_pk_fp8_f32 v134, v72, v76 op_sel:[0,0,1]
	s_waitcnt vmcnt(17)
	v_mul_f32_e32 v72, 0x42800000, v112
	s_waitcnt vmcnt(16)
	v_mul_f32_e32 v76, 0x42800000, v124
	v_cvt_pk_fp8_f32 v135, v72, v76 op_sel:[0,0,1]
	v_mul_f32_e32 v2, 0x42800000, v69
	v_mul_f32_e32 v68, 0x42800000, v77
	v_mul_f32_e32 v69, 0x42800000, v81
	global_store_dwordx4 v[142:143], v[132:135], off nt
	v_mul_f32_e32 v72, 0x42800000, v105
	v_or_b32_e32 v142, 32, v138
	v_mov_b32_e32 v132, v3
	v_cvt_pk_fp8_f32 v132, v2, v68
	v_mul_f32_e32 v2, 0x42800000, v85
	v_mul_f32_e32 v68, 0x42800000, v109
	v_mov_b32_e32 v133, v3
	v_cvt_pk_fp8_f32 v133, v2, v68
	v_mul_f32_e32 v2, 0x42800000, v73
	v_mul_f32_e32 v68, 0x42800000, v93
	v_mov_b32_e32 v134, v3
	v_cvt_pk_fp8_f32 v134, v2, v68
	v_mul_f32_e32 v2, 0x42800000, v89
	v_mul_f32_e32 v68, 0x42800000, v101
	v_mov_b32_e32 v135, v3
	v_cvt_pk_fp8_f32 v135, v2, v68
	v_cvt_pk_fp8_f32 v132, v69, v72 op_sel:[0,0,1]
	v_mul_f32_e32 v69, 0x42800000, v117
	v_mul_f32_e32 v72, 0x42800000, v129
	v_cvt_pk_fp8_f32 v133, v69, v72 op_sel:[0,0,1]
	v_mul_f32_e32 v69, 0x42800000, v97
	v_mul_f32_e32 v72, 0x42800000, v121
	v_cvt_pk_fp8_f32 v134, v69, v72 op_sel:[0,0,1]
	v_mul_f32_e32 v69, 0x42800000, v113
	v_mul_f32_e32 v72, 0x42800000, v125
	v_cvt_pk_fp8_f32 v135, v69, v72 op_sel:[0,0,1]
	v_or_b32_e32 v68, 1, v138
	v_ashrrev_i32_e32 v69, 31, v68
	v_lshlrev_b64 v[68:69], 11, v[68:69]
	v_lshl_add_u64 v[68:69], v[136:137], 0, v[68:69]
	global_store_dwordx4 v[68:69], v[132:135], off nt
	v_mul_f32_e32 v2, 0x42800000, v70
	v_mul_f32_e32 v68, 0x42800000, v78
	v_mov_b32_e32 v132, v3
	v_cvt_pk_fp8_f32 v132, v2, v68
	v_mul_f32_e32 v2, 0x42800000, v86
	v_mul_f32_e32 v68, 0x42800000, v110
	v_mov_b32_e32 v133, v3
	v_cvt_pk_fp8_f32 v133, v2, v68
	v_mul_f32_e32 v2, 0x42800000, v74
	v_mul_f32_e32 v68, 0x42800000, v94
	v_mov_b32_e32 v134, v3
	v_cvt_pk_fp8_f32 v134, v2, v68
	v_mul_f32_e32 v2, 0x42800000, v90
	v_mul_f32_e32 v68, 0x42800000, v102
	v_mov_b32_e32 v135, v3
	v_mul_f32_e32 v69, 0x42800000, v82
	v_mul_f32_e32 v70, 0x42800000, v106
	v_cvt_pk_fp8_f32 v135, v2, v68
	v_cvt_pk_fp8_f32 v132, v69, v70 op_sel:[0,0,1]
	v_mul_f32_e32 v69, 0x42800000, v118
	v_mul_f32_e32 v70, 0x42800000, v130
	v_cvt_pk_fp8_f32 v133, v69, v70 op_sel:[0,0,1]
	v_mul_f32_e32 v69, 0x42800000, v98
	v_mul_f32_e32 v70, 0x42800000, v122
	v_cvt_pk_fp8_f32 v134, v69, v70 op_sel:[0,0,1]
	v_mul_f32_e32 v69, 0x42800000, v114
	v_mul_f32_e32 v70, 0x42800000, v126
	v_cvt_pk_fp8_f32 v135, v69, v70 op_sel:[0,0,1]
	v_or_b32_e32 v68, 2, v138
	v_ashrrev_i32_e32 v69, 31, v68
	v_lshlrev_b64 v[68:69], 11, v[68:69]
	v_lshl_add_u64 v[68:69], v[136:137], 0, v[68:69]
	global_store_dwordx4 v[68:69], v[132:135], off nt
	v_mul_f32_e32 v2, 0x42800000, v71
	v_mul_f32_e32 v69, 0x42800000, v79
	v_mov_b32_e32 v68, v3
	v_cvt_pk_fp8_f32 v68, v2, v69
	v_mul_f32_e32 v70, 0x42800000, v83
	v_mul_f32_e32 v71, 0x42800000, v107
	v_mul_f32_e32 v2, 0x42800000, v87
	v_cvt_pk_fp8_f32 v68, v70, v71 op_sel:[0,0,1]
	v_mul_f32_e32 v70, 0x42800000, v111
	v_mov_b32_e32 v69, v3
	v_cvt_pk_fp8_f32 v69, v2, v70
	v_mul_f32_e32 v71, 0x42800000, v119
	v_mul_f32_e32 v72, 0x42800000, v131
	v_mul_f32_e32 v2, 0x42800000, v75
	v_cvt_pk_fp8_f32 v69, v71, v72 op_sel:[0,0,1]
	v_mul_f32_e32 v71, 0x42800000, v95
	v_mov_b32_e32 v70, v3
	v_cvt_pk_fp8_f32 v70, v2, v71
	v_mul_f32_e32 v72, 0x42800000, v99
	v_mul_f32_e32 v73, 0x42800000, v123
	v_mul_f32_e32 v2, 0x42800000, v91
	v_cvt_pk_fp8_f32 v70, v72, v73 op_sel:[0,0,1]
	v_mul_f32_e32 v72, 0x42800000, v103
	v_mov_b32_e32 v71, v3
	v_cvt_pk_fp8_f32 v71, v2, v72
	v_mul_f32_e32 v73, 0x42800000, v115
	v_mul_f32_e32 v74, 0x42800000, v127
	v_or_b32_e32 v72, 3, v138
	v_cvt_pk_fp8_f32 v71, v73, v74 op_sel:[0,0,1]
	v_ashrrev_i32_e32 v73, 31, v72
	v_lshlrev_b64 v[72:73], 11, v[72:73]
	v_lshl_add_u64 v[72:73], v[136:137], 0, v[72:73]
	global_store_dwordx4 v[72:73], v[68:71], off nt
	s_waitcnt vmcnt(19)
	v_mul_f32_e32 v2, 0x42800000, v52
	s_waitcnt vmcnt(18)
	v_mul_f32_e32 v52, 0x42800000, v56
	v_mov_b32_e32 v132, v3
	buffer_load_dwordx4 v[116:119], v140, s[24:27], s3 offen offset:256 sc0 sc1 nt
	buffer_load_dwordx4 v[120:123], v140, s[24:27], s14 offen offset:256 sc0 sc1 nt
	buffer_load_dwordx4 v[124:127], v140, s[24:27], s15 offen offset:256 sc0 sc1 nt
	buffer_load_dwordx4 v[128:131], v140, s[24:27], s16 offen offset:256 sc0 sc1 nt
	buffer_load_dwordx4 v[100:103], v140, s[24:27], s17 offen offset:256 sc0 sc1 nt
	buffer_load_dwordx4 v[104:107], v140, s[24:27], s18 offen offset:256 sc0 sc1 nt
	buffer_load_dwordx4 v[108:111], v140, s[24:27], s19 offen offset:256 sc0 sc1 nt
	buffer_load_dwordx4 v[112:115], v140, s[24:27], s22 offen offset:256 sc0 sc1 nt
	buffer_load_dwordx4 v[84:87], v140, s[24:27], s2 offen offset:256 sc0 sc1 nt
	buffer_load_dwordx4 v[88:91], v140, s[24:27], s33 offen offset:256 sc0 sc1 nt
	buffer_load_dwordx4 v[92:95], v140, s[24:27], s40 offen offset:256 sc0 sc1 nt
	buffer_load_dwordx4 v[96:99], v140, s[24:27], s41 offen offset:256 sc0 sc1 nt
	buffer_load_dwordx4 v[68:71], v140, s[24:27], s42 offen offset:256 sc0 sc1 nt
	buffer_load_dwordx4 v[72:75], v140, s[24:27], s43 offen offset:256 sc0 sc1 nt
	buffer_load_dwordx4 v[76:79], v140, s[24:27], s46 offen offset:256 sc0 sc1 nt
	buffer_load_dwordx4 v[80:83], v140, s[24:27], s47 offen offset:256 sc0 sc1 nt
	v_cvt_pk_fp8_f32 v132, v2, v52
	s_waitcnt vmcnt(31)
	v_mul_f32_e32 v2, 0x42800000, v36
	s_waitcnt vmcnt(30)
	v_mul_f32_e32 v36, 0x42800000, v40
	v_mov_b32_e32 v133, v3
	v_cvt_pk_fp8_f32 v133, v2, v36
	s_waitcnt vmcnt(27)
	v_mul_f32_e32 v2, 0x42800000, v20
	s_waitcnt vmcnt(26)
	v_mul_f32_e32 v20, 0x42800000, v24
	v_mov_b32_e32 v134, v3
	v_cvt_pk_fp8_f32 v134, v2, v20
	s_waitcnt vmcnt(23)
	v_mul_f32_e32 v2, 0x42800000, v4
	s_waitcnt vmcnt(22)
	v_mul_f32_e32 v4, 0x42800000, v8
	v_mov_b32_e32 v135, v3
	v_cvt_pk_fp8_f32 v135, v2, v4
	v_mul_f32_e32 v56, 0x42800000, v60
	v_mul_f32_e32 v60, 0x42800000, v64
	v_mul_f32_e32 v40, 0x42800000, v44
	v_mul_f32_e32 v44, 0x42800000, v48
	v_mul_f32_e32 v24, 0x42800000, v28
	v_mul_f32_e32 v28, 0x42800000, v32
	s_waitcnt vmcnt(21)
	v_mul_f32_e32 v8, 0x42800000, v12
	s_waitcnt vmcnt(20)
	v_mul_f32_e32 v12, 0x42800000, v16
	v_cvt_pk_fp8_f32 v132, v56, v60 op_sel:[0,0,1]
	v_cvt_pk_fp8_f32 v133, v40, v44 op_sel:[0,0,1]
	v_cvt_pk_fp8_f32 v134, v24, v28 op_sel:[0,0,1]
	v_cvt_pk_fp8_f32 v135, v8, v12 op_sel:[0,0,1]
	v_ashrrev_i32_e32 v143, 31, v142
	v_lshlrev_b64 v[142:143], 11, v[142:143]
	v_lshl_add_u64 v[142:143], v[136:137], 0, v[142:143]
	global_store_dwordx4 v[142:143], v[132:135], off nt
	v_mul_f32_e32 v2, 0x42800000, v53
	v_mul_f32_e32 v4, 0x42800000, v57
	v_mov_b32_e32 v132, v3
	v_cvt_pk_fp8_f32 v132, v2, v4
	v_mul_f32_e32 v2, 0x42800000, v37
	v_mul_f32_e32 v4, 0x42800000, v41
	v_mov_b32_e32 v133, v3
	v_cvt_pk_fp8_f32 v133, v2, v4
	v_mul_f32_e32 v2, 0x42800000, v21
	v_mul_f32_e32 v4, 0x42800000, v25
	v_mov_b32_e32 v134, v3
	v_cvt_pk_fp8_f32 v134, v2, v4
	v_mul_f32_e32 v2, 0x42800000, v5
	v_mul_f32_e32 v4, 0x42800000, v9
	v_mov_b32_e32 v135, v3
	v_mul_f32_e32 v8, 0x42800000, v61
	v_mul_f32_e32 v12, 0x42800000, v65
	v_cvt_pk_fp8_f32 v135, v2, v4
	v_cvt_pk_fp8_f32 v132, v8, v12 op_sel:[0,0,1]
	v_mul_f32_e32 v8, 0x42800000, v45
	v_mul_f32_e32 v12, 0x42800000, v49
	v_cvt_pk_fp8_f32 v133, v8, v12 op_sel:[0,0,1]
	v_mul_f32_e32 v8, 0x42800000, v29
	v_mul_f32_e32 v12, 0x42800000, v33
	v_cvt_pk_fp8_f32 v134, v8, v12 op_sel:[0,0,1]
	v_mul_f32_e32 v5, 0x42800000, v13
	v_mul_f32_e32 v8, 0x42800000, v17
	v_cvt_pk_fp8_f32 v135, v5, v8 op_sel:[0,0,1]
	v_or_b32_e32 v4, 33, v138
	v_ashrrev_i32_e32 v5, 31, v4
	v_lshlrev_b64 v[4:5], 11, v[4:5]
	v_lshl_add_u64 v[4:5], v[136:137], 0, v[4:5]
	global_store_dwordx4 v[4:5], v[132:135], off nt
	v_mul_f32_e32 v2, 0x42800000, v54
	v_mul_f32_e32 v4, 0x42800000, v58
	v_mov_b32_e32 v132, v3
	v_cvt_pk_fp8_f32 v132, v2, v4
	v_mul_f32_e32 v2, 0x42800000, v38
	v_mul_f32_e32 v4, 0x42800000, v42
	v_mov_b32_e32 v133, v3
	v_cvt_pk_fp8_f32 v133, v2, v4
	v_mul_f32_e32 v2, 0x42800000, v22
	v_mul_f32_e32 v4, 0x42800000, v26
	v_mov_b32_e32 v134, v3
	v_cvt_pk_fp8_f32 v134, v2, v4
	v_mul_f32_e32 v2, 0x42800000, v6
	v_mul_f32_e32 v4, 0x42800000, v10
	v_mov_b32_e32 v135, v3
	v_mul_f32_e32 v5, 0x42800000, v62
	v_mul_f32_e32 v8, 0x42800000, v66
	v_cvt_pk_fp8_f32 v135, v2, v4
	v_cvt_pk_fp8_f32 v132, v5, v8 op_sel:[0,0,1]
	v_mul_f32_e32 v5, 0x42800000, v46
	v_mul_f32_e32 v8, 0x42800000, v50
	v_cvt_pk_fp8_f32 v133, v5, v8 op_sel:[0,0,1]
	v_mul_f32_e32 v5, 0x42800000, v30
	v_mul_f32_e32 v8, 0x42800000, v34
	v_cvt_pk_fp8_f32 v134, v5, v8 op_sel:[0,0,1]
	v_mul_f32_e32 v5, 0x42800000, v14
	v_mul_f32_e32 v6, 0x42800000, v18
	v_cvt_pk_fp8_f32 v135, v5, v6 op_sel:[0,0,1]
	v_or_b32_e32 v4, 34, v138
	v_ashrrev_i32_e32 v5, 31, v4
	v_lshlrev_b64 v[4:5], 11, v[4:5]
	v_lshl_add_u64 v[4:5], v[136:137], 0, v[4:5]
	global_store_dwordx4 v[4:5], v[132:135], off nt
	v_mul_f32_e32 v2, 0x42800000, v55
	v_mul_f32_e32 v5, 0x42800000, v59
	v_mov_b32_e32 v4, v3
	v_cvt_pk_fp8_f32 v4, v2, v5
	v_mul_f32_e32 v6, 0x42800000, v63
	v_mul_f32_e32 v8, 0x42800000, v67
	v_mul_f32_e32 v2, 0x42800000, v39
	v_cvt_pk_fp8_f32 v4, v6, v8 op_sel:[0,0,1]
	v_mul_f32_e32 v6, 0x42800000, v43
	v_mov_b32_e32 v5, v3
	v_cvt_pk_fp8_f32 v5, v2, v6
	v_mul_f32_e32 v8, 0x42800000, v47
	v_mul_f32_e32 v9, 0x42800000, v51
	v_mul_f32_e32 v2, 0x42800000, v23
	v_cvt_pk_fp8_f32 v5, v8, v9 op_sel:[0,0,1]
	v_mul_f32_e32 v8, 0x42800000, v27
	v_mov_b32_e32 v6, v3
	v_cvt_pk_fp8_f32 v6, v2, v8
	v_mul_f32_e32 v2, 0x42800000, v7
	v_mul_f32_e32 v8, 0x42800000, v11
	v_mov_b32_e32 v7, v3
	v_cvt_pk_fp8_f32 v7, v2, v8
	v_mul_f32_e32 v9, 0x42800000, v31
	v_mul_f32_e32 v10, 0x42800000, v35
	v_cvt_pk_fp8_f32 v6, v9, v10 op_sel:[0,0,1]
	v_mul_f32_e32 v9, 0x42800000, v15
	v_mul_f32_e32 v10, 0x42800000, v19
	v_cvt_pk_fp8_f32 v7, v9, v10 op_sel:[0,0,1]
	v_or_b32_e32 v8, 35, v138
	v_ashrrev_i32_e32 v9, 31, v8
	v_lshlrev_b64 v[8:9], 11, v[8:9]
	v_lshl_add_u64 v[8:9], v[136:137], 0, v[8:9]
	global_store_dwordx4 v[8:9], v[4:7], off nt
	buffer_load_dwordx4 v[52:55], v140, s[24:27], s3 offen offset:384 sc0 sc1 nt
	buffer_load_dwordx4 v[56:59], v140, s[24:27], s14 offen offset:384 sc0 sc1 nt
	buffer_load_dwordx4 v[60:63], v140, s[24:27], s15 offen offset:384 sc0 sc1 nt
	buffer_load_dwordx4 v[64:67], v140, s[24:27], s16 offen offset:384 sc0 sc1 nt
	buffer_load_dwordx4 v[36:39], v140, s[24:27], s17 offen offset:384 sc0 sc1 nt
	buffer_load_dwordx4 v[40:43], v140, s[24:27], s18 offen offset:384 sc0 sc1 nt
	buffer_load_dwordx4 v[44:47], v140, s[24:27], s19 offen offset:384 sc0 sc1 nt
	buffer_load_dwordx4 v[48:51], v140, s[24:27], s22 offen offset:384 sc0 sc1 nt
	buffer_load_dwordx4 v[20:23], v140, s[24:27], s2 offen offset:384 sc0 sc1 nt
	buffer_load_dwordx4 v[24:27], v140, s[24:27], s33 offen offset:384 sc0 sc1 nt
	buffer_load_dwordx4 v[28:31], v140, s[24:27], s40 offen offset:384 sc0 sc1 nt
	buffer_load_dwordx4 v[32:35], v140, s[24:27], s41 offen offset:384 sc0 sc1 nt
	buffer_load_dwordx4 v[4:7], v140, s[24:27], s42 offen offset:384 sc0 sc1 nt
	buffer_load_dwordx4 v[8:11], v140, s[24:27], s43 offen offset:384 sc0 sc1 nt
	buffer_load_dwordx4 v[12:15], v140, s[24:27], s46 offen offset:384 sc0 sc1 nt
	buffer_load_dwordx4 v[16:19], v140, s[24:27], s47 offen offset:384 sc0 sc1 nt
	s_waitcnt vmcnt(35)
	v_mul_f32_e32 v2, 0x42800000, v116
	s_waitcnt vmcnt(34)
	v_mul_f32_e32 v116, 0x42800000, v120
	v_mov_b32_e32 v132, v3
	v_cvt_pk_fp8_f32 v132, v2, v116
	s_waitcnt vmcnt(31)
	v_mul_f32_e32 v2, 0x42800000, v100
	s_waitcnt vmcnt(30)
	v_mul_f32_e32 v100, 0x42800000, v104
	v_mov_b32_e32 v133, v3
	v_cvt_pk_fp8_f32 v133, v2, v100
	s_waitcnt vmcnt(27)
	v_mul_f32_e32 v2, 0x42800000, v84
	s_waitcnt vmcnt(26)
	v_mul_f32_e32 v84, 0x42800000, v88
	v_mov_b32_e32 v134, v3
	v_cvt_pk_fp8_f32 v134, v2, v84
	s_waitcnt vmcnt(23)
	v_mul_f32_e32 v2, 0x42800000, v68
	s_waitcnt vmcnt(22)
	v_mul_f32_e32 v68, 0x42800000, v72
	v_mov_b32_e32 v135, v3
	v_cvt_pk_fp8_f32 v135, v2, v68
	v_mul_f32_e32 v120, 0x42800000, v124
	v_mul_f32_e32 v124, 0x42800000, v128
	v_mul_f32_e32 v104, 0x42800000, v108
	v_mul_f32_e32 v108, 0x42800000, v112
	v_mul_f32_e32 v88, 0x42800000, v92
	v_mul_f32_e32 v92, 0x42800000, v96
	s_waitcnt vmcnt(21)
	v_mul_f32_e32 v72, 0x42800000, v76
	s_waitcnt vmcnt(20)
	v_mul_f32_e32 v76, 0x42800000, v80
	v_cvt_pk_fp8_f32 v132, v120, v124 op_sel:[0,0,1]
	v_cvt_pk_fp8_f32 v133, v104, v108 op_sel:[0,0,1]
	v_cvt_pk_fp8_f32 v134, v88, v92 op_sel:[0,0,1]
	v_cvt_pk_fp8_f32 v135, v72, v76 op_sel:[0,0,1]
	v_or_b32_e32 v140, 64, v138
	v_ashrrev_i32_e32 v141, 31, v140
	v_lshlrev_b64 v[140:141], 11, v[140:141]
	v_lshl_add_u64 v[140:141], v[136:137], 0, v[140:141]
	global_store_dwordx4 v[140:141], v[132:135], off nt
	v_mul_f32_e32 v2, 0x42800000, v117
	v_mul_f32_e32 v68, 0x42800000, v121
	v_mov_b32_e32 v132, v3
	v_cvt_pk_fp8_f32 v132, v2, v68
	v_mul_f32_e32 v2, 0x42800000, v101
	v_mul_f32_e32 v68, 0x42800000, v105
	v_mov_b32_e32 v133, v3
	v_cvt_pk_fp8_f32 v133, v2, v68
	v_mul_f32_e32 v2, 0x42800000, v85
	v_mul_f32_e32 v68, 0x42800000, v89
	v_mov_b32_e32 v134, v3
	v_cvt_pk_fp8_f32 v134, v2, v68
	v_mul_f32_e32 v2, 0x42800000, v69
	v_mul_f32_e32 v68, 0x42800000, v73
	v_mov_b32_e32 v135, v3
	v_mul_f32_e32 v72, 0x42800000, v125
	v_mul_f32_e32 v76, 0x42800000, v129
	v_cvt_pk_fp8_f32 v135, v2, v68
	v_cvt_pk_fp8_f32 v132, v72, v76 op_sel:[0,0,1]
	v_mul_f32_e32 v72, 0x42800000, v109
	v_mul_f32_e32 v76, 0x42800000, v113
	v_cvt_pk_fp8_f32 v133, v72, v76 op_sel:[0,0,1]
	v_mul_f32_e32 v72, 0x42800000, v93
	v_mul_f32_e32 v76, 0x42800000, v97
	v_cvt_pk_fp8_f32 v134, v72, v76 op_sel:[0,0,1]
	v_mul_f32_e32 v69, 0x42800000, v77
	v_mul_f32_e32 v72, 0x42800000, v81
	v_cvt_pk_fp8_f32 v135, v69, v72 op_sel:[0,0,1]
	v_or_b32_e32 v68, 0x41, v138
	v_ashrrev_i32_e32 v69, 31, v68
	v_lshlrev_b64 v[68:69], 11, v[68:69]
	v_lshl_add_u64 v[68:69], v[136:137], 0, v[68:69]
	global_store_dwordx4 v[68:69], v[132:135], off nt
	v_mul_f32_e32 v2, 0x42800000, v118
	v_mul_f32_e32 v68, 0x42800000, v122
	v_mov_b32_e32 v132, v3
	v_cvt_pk_fp8_f32 v132, v2, v68
	v_mul_f32_e32 v2, 0x42800000, v102
	v_mul_f32_e32 v68, 0x42800000, v106
	v_mov_b32_e32 v133, v3
	v_cvt_pk_fp8_f32 v133, v2, v68
	v_mul_f32_e32 v2, 0x42800000, v86
	v_mul_f32_e32 v68, 0x42800000, v90
	v_mov_b32_e32 v134, v3
	v_cvt_pk_fp8_f32 v134, v2, v68
	v_mul_f32_e32 v2, 0x42800000, v70
	v_mul_f32_e32 v68, 0x42800000, v74
	v_mov_b32_e32 v135, v3
	v_mul_f32_e32 v69, 0x42800000, v126
	v_mul_f32_e32 v72, 0x42800000, v130
	v_cvt_pk_fp8_f32 v135, v2, v68
	v_cvt_pk_fp8_f32 v132, v69, v72 op_sel:[0,0,1]
	v_mul_f32_e32 v69, 0x42800000, v110
	v_mul_f32_e32 v72, 0x42800000, v114
	v_cvt_pk_fp8_f32 v133, v69, v72 op_sel:[0,0,1]
	v_mul_f32_e32 v69, 0x42800000, v94
	v_mul_f32_e32 v72, 0x42800000, v98
	v_cvt_pk_fp8_f32 v134, v69, v72 op_sel:[0,0,1]
	v_mul_f32_e32 v69, 0x42800000, v78
	v_mul_f32_e32 v70, 0x42800000, v82
	v_cvt_pk_fp8_f32 v135, v69, v70 op_sel:[0,0,1]
	v_or_b32_e32 v68, 0x42, v138
	v_ashrrev_i32_e32 v69, 31, v68
	v_lshlrev_b64 v[68:69], 11, v[68:69]
	v_lshl_add_u64 v[68:69], v[136:137], 0, v[68:69]
	global_store_dwordx4 v[68:69], v[132:135], off nt
	v_mul_f32_e32 v2, 0x42800000, v119
	v_mul_f32_e32 v69, 0x42800000, v123
	v_mov_b32_e32 v68, v3
	v_cvt_pk_fp8_f32 v68, v2, v69
	v_mul_f32_e32 v70, 0x42800000, v127
	v_mul_f32_e32 v72, 0x42800000, v131
	v_mul_f32_e32 v2, 0x42800000, v103
	v_cvt_pk_fp8_f32 v68, v70, v72 op_sel:[0,0,1]
	v_mul_f32_e32 v70, 0x42800000, v107
	v_mov_b32_e32 v69, v3
	v_cvt_pk_fp8_f32 v69, v2, v70
	v_mul_f32_e32 v72, 0x42800000, v111
	v_mul_f32_e32 v73, 0x42800000, v115
	v_mul_f32_e32 v2, 0x42800000, v87
	v_cvt_pk_fp8_f32 v69, v72, v73 op_sel:[0,0,1]
	v_mul_f32_e32 v72, 0x42800000, v91
	v_mov_b32_e32 v70, v3
	v_cvt_pk_fp8_f32 v70, v2, v72
	v_mul_f32_e32 v2, 0x42800000, v71
	v_mul_f32_e32 v72, 0x42800000, v75
	v_mov_b32_e32 v71, v3
	v_cvt_pk_fp8_f32 v71, v2, v72
	v_mul_f32_e32 v73, 0x42800000, v95
	v_mul_f32_e32 v74, 0x42800000, v99
	v_cvt_pk_fp8_f32 v70, v73, v74 op_sel:[0,0,1]
	v_mul_f32_e32 v73, 0x42800000, v79
	v_mul_f32_e32 v74, 0x42800000, v83
	v_cvt_pk_fp8_f32 v71, v73, v74 op_sel:[0,0,1]
	v_or_b32_e32 v72, 0x43, v138
	v_ashrrev_i32_e32 v73, 31, v72
	v_lshlrev_b64 v[72:73], 11, v[72:73]
	v_lshl_add_u64 v[72:73], v[136:137], 0, v[72:73]
	global_store_dwordx4 v[72:73], v[68:71], off nt
	s_waitcnt vmcnt(19)
	v_mul_f32_e32 v2, 0x42800000, v52
	s_waitcnt vmcnt(18)
	v_mul_f32_e32 v52, 0x42800000, v56
	v_mov_b32_e32 v68, v3
	v_cvt_pk_fp8_f32 v68, v2, v52
	s_waitcnt vmcnt(15)
	v_mul_f32_e32 v2, 0x42800000, v36
	s_waitcnt vmcnt(14)
	v_mul_f32_e32 v36, 0x42800000, v40
	v_mov_b32_e32 v69, v3
	v_cvt_pk_fp8_f32 v69, v2, v36
	s_waitcnt vmcnt(11)
	v_mul_f32_e32 v2, 0x42800000, v20
	s_waitcnt vmcnt(10)
	v_mul_f32_e32 v20, 0x42800000, v24
	v_mov_b32_e32 v70, v3
	v_cvt_pk_fp8_f32 v70, v2, v20
	s_waitcnt vmcnt(7)
	v_mul_f32_e32 v2, 0x42800000, v4
	s_waitcnt vmcnt(6)
	v_mul_f32_e32 v4, 0x42800000, v8
	v_mov_b32_e32 v71, v3
	v_cvt_pk_fp8_f32 v71, v2, v4
	v_mul_f32_e32 v56, 0x42800000, v60
	v_mul_f32_e32 v60, 0x42800000, v64
	v_mul_f32_e32 v40, 0x42800000, v44
	v_mul_f32_e32 v44, 0x42800000, v48
	v_mul_f32_e32 v24, 0x42800000, v28
	v_mul_f32_e32 v28, 0x42800000, v32
	s_waitcnt vmcnt(5)
	v_mul_f32_e32 v8, 0x42800000, v12
	s_waitcnt vmcnt(4)
	v_mul_f32_e32 v12, 0x42800000, v16
	v_cvt_pk_fp8_f32 v68, v56, v60 op_sel:[0,0,1]
	v_cvt_pk_fp8_f32 v69, v40, v44 op_sel:[0,0,1]
	v_cvt_pk_fp8_f32 v70, v24, v28 op_sel:[0,0,1]
	v_cvt_pk_fp8_f32 v71, v8, v12 op_sel:[0,0,1]
	v_or_b32_e32 v72, 0x60, v138
	v_ashrrev_i32_e32 v73, 31, v72
	v_lshlrev_b64 v[72:73], 11, v[72:73]
	v_lshl_add_u64 v[72:73], v[136:137], 0, v[72:73]
	global_store_dwordx4 v[72:73], v[68:71], off nt
	v_mul_f32_e32 v2, 0x42800000, v53
	v_mul_f32_e32 v4, 0x42800000, v57
	v_mov_b32_e32 v68, v3
	v_cvt_pk_fp8_f32 v68, v2, v4
	v_mul_f32_e32 v2, 0x42800000, v37
	v_mul_f32_e32 v4, 0x42800000, v41
	v_mov_b32_e32 v69, v3
	v_cvt_pk_fp8_f32 v69, v2, v4
	v_mul_f32_e32 v2, 0x42800000, v21
	v_mul_f32_e32 v4, 0x42800000, v25
	v_mov_b32_e32 v70, v3
	v_cvt_pk_fp8_f32 v70, v2, v4
	v_mul_f32_e32 v2, 0x42800000, v5
	v_mul_f32_e32 v4, 0x42800000, v9
	v_mov_b32_e32 v71, v3
	v_mul_f32_e32 v8, 0x42800000, v61
	v_mul_f32_e32 v12, 0x42800000, v65
	v_cvt_pk_fp8_f32 v71, v2, v4
	v_cvt_pk_fp8_f32 v68, v8, v12 op_sel:[0,0,1]
	v_mul_f32_e32 v8, 0x42800000, v45
	v_mul_f32_e32 v12, 0x42800000, v49
	v_cvt_pk_fp8_f32 v69, v8, v12 op_sel:[0,0,1]
	v_mul_f32_e32 v8, 0x42800000, v29
	v_mul_f32_e32 v12, 0x42800000, v33
	v_cvt_pk_fp8_f32 v70, v8, v12 op_sel:[0,0,1]
	v_mul_f32_e32 v5, 0x42800000, v13
	v_mul_f32_e32 v8, 0x42800000, v17
	v_cvt_pk_fp8_f32 v71, v5, v8 op_sel:[0,0,1]
	v_or_b32_e32 v4, 0x61, v138
	v_ashrrev_i32_e32 v5, 31, v4
	v_lshlrev_b64 v[4:5], 11, v[4:5]
	v_lshl_add_u64 v[4:5], v[136:137], 0, v[4:5]
	global_store_dwordx4 v[4:5], v[68:71], off nt
	v_mul_f32_e32 v2, 0x42800000, v54
	v_mul_f32_e32 v4, 0x42800000, v58
	v_mov_b32_e32 v68, v3
	v_cvt_pk_fp8_f32 v68, v2, v4
	v_mul_f32_e32 v2, 0x42800000, v38
	v_mul_f32_e32 v4, 0x42800000, v42
	v_mov_b32_e32 v69, v3
	v_cvt_pk_fp8_f32 v69, v2, v4
	v_mul_f32_e32 v2, 0x42800000, v22
	v_mul_f32_e32 v4, 0x42800000, v26
	v_mov_b32_e32 v70, v3
	v_cvt_pk_fp8_f32 v70, v2, v4
	v_mul_f32_e32 v2, 0x42800000, v6
	v_mul_f32_e32 v4, 0x42800000, v10
	v_mov_b32_e32 v71, v3
	v_mul_f32_e32 v5, 0x42800000, v62
	v_mul_f32_e32 v8, 0x42800000, v66
	v_cvt_pk_fp8_f32 v71, v2, v4
	v_cvt_pk_fp8_f32 v68, v5, v8 op_sel:[0,0,1]
	v_mul_f32_e32 v5, 0x42800000, v46
	v_mul_f32_e32 v8, 0x42800000, v50
	v_cvt_pk_fp8_f32 v69, v5, v8 op_sel:[0,0,1]
	v_mul_f32_e32 v5, 0x42800000, v30
	v_mul_f32_e32 v8, 0x42800000, v34
	v_cvt_pk_fp8_f32 v70, v5, v8 op_sel:[0,0,1]
	v_mul_f32_e32 v5, 0x42800000, v14
	v_mul_f32_e32 v6, 0x42800000, v18
	v_cvt_pk_fp8_f32 v71, v5, v6 op_sel:[0,0,1]
	v_or_b32_e32 v4, 0x62, v138
	v_ashrrev_i32_e32 v5, 31, v4
	v_lshlrev_b64 v[4:5], 11, v[4:5]
	v_lshl_add_u64 v[4:5], v[136:137], 0, v[4:5]
	global_store_dwordx4 v[4:5], v[68:71], off nt
	v_mul_f32_e32 v2, 0x42800000, v55
	v_mul_f32_e32 v5, 0x42800000, v59
	v_mov_b32_e32 v4, v3
	v_cvt_pk_fp8_f32 v4, v2, v5
	v_mul_f32_e32 v6, 0x42800000, v63
	v_mul_f32_e32 v8, 0x42800000, v67
	v_mul_f32_e32 v2, 0x42800000, v39
	v_cvt_pk_fp8_f32 v4, v6, v8 op_sel:[0,0,1]
	v_mul_f32_e32 v6, 0x42800000, v43
	v_mov_b32_e32 v5, v3
	v_cvt_pk_fp8_f32 v5, v2, v6
	v_mul_f32_e32 v8, 0x42800000, v47
	v_mul_f32_e32 v9, 0x42800000, v51
	v_mul_f32_e32 v2, 0x42800000, v23
	v_cvt_pk_fp8_f32 v5, v8, v9 op_sel:[0,0,1]
	v_mul_f32_e32 v8, 0x42800000, v27
	v_mov_b32_e32 v6, v3
	v_cvt_pk_fp8_f32 v6, v2, v8
	v_mul_f32_e32 v2, 0x42800000, v7
	v_mul_f32_e32 v8, 0x42800000, v11
	v_mov_b32_e32 v7, v3
	v_cvt_pk_fp8_f32 v7, v2, v8
	v_mul_f32_e32 v9, 0x42800000, v31
	v_mul_f32_e32 v10, 0x42800000, v35
	v_cvt_pk_fp8_f32 v6, v9, v10 op_sel:[0,0,1]
	v_mul_f32_e32 v9, 0x42800000, v15
	v_mul_f32_e32 v10, 0x42800000, v19
	v_cvt_pk_fp8_f32 v7, v9, v10 op_sel:[0,0,1]
	v_or_b32_e32 v8, 0x63, v138
	s_mov_b64 s[16:17], 11
